# P2 split 157 GEMM / 99 quantizer workgroups (17 GEMM rounds with a full last round); otherwise v84
# baseline (speedup 1.0000x reference)
; #define Q_GRAB() (((stop != nullptr && xb_ld(stop) >= thr) || (quota > 0 && qleft-- <= 0)) ? (unsigned)hi : (unsigned)lo + atomicAdd(cnt, 1u))
;     ...
;     __syncthreads();
;     if (tid == 0) MISC[2] = Q_GRAB();
; __global__ void __launch_bounds__(NWAVES * 64, 2) fwd_kernel(Args a_unused) {
;     ...
;         constexpr int GA = 160, NUN = (MROWS / 256) * (INC / 256);
;         const int Gact = (G == 256) ? GA : G;
;         if (bx >= Gact) {
;             quant_queue(A, ws, ctl, lds, MISC, ctl + CW_QE, QN0, QN0 + 6144, ctl + CW_DONE, (unsigned)((NUN % GA) ? GA - NUN % GA + 1 : 1));
.LBB0_302:
	s_cmp_lt_i32 s46, 3
	s_cselect_b64 s[6:7], -1, 0
	s_and_b64 s[14:15], s[6:7], s[4:5]
	s_andn2_b64 vcc, exec, s[14:15]
	s_cbranch_vccnz .LBB0_1126
	s_mov_b64 s[18:19], s[0:1]
	s_load_dwordx2 s[16:17], s[18:19], 0xc8
	s_cmpk_lg_i32 s33, 0x100
	s_cselect_b32 s57, s33, 0x9d
	s_cmp_lt_i32 s2, s57
	s_mov_b64 s[4:5], -1
	s_cbranch_scc1 .LBB0_446
	s_add_u32 s20, s48, 0x9100
	s_addc_u32 s21, s49, 0
	s_add_u32 s22, s48, 0x9200
	s_addc_u32 s23, s49, 0
	v_readfirstlane_b32 s12, v0
	s_waitcnt lgkmcnt(0)
	s_barrier
	s_and_saveexec_b64 s[4:5], s[40:41]
	s_cbranch_execz .LBB0_310
	v_mov_b32_e32 v1, 0
	global_load_dword v1, v1, s[22:23] sc1
	s_waitcnt vmcnt(0)
	v_cmp_lt_u32_e32 vcc, 4, v1
	v_mov_b32_e32 v1, 0x19c8
	s_cbranch_vccnz .LBB0_309
	s_mov_b64 s[8:9], exec
	v_mbcnt_lo_u32_b32 v1, s8, 0
	v_mbcnt_hi_u32_b32 v1, s9, v1
	v_cmp_eq_u32_e32 vcc, 0, v1
	s_and_saveexec_b64 s[6:7], vcc
	s_cbranch_execz .LBB0_308
	s_bcnt1_i32_b64 s3, s[8:9]
	v_mov_b32_e32 v2, 0
	v_mov_b32_e32 v3, s3
	global_atomic_add v2, v2, v3, s[20:21] sc0

; #define LAS __attribute__((address_space(3)))
; #define Q_GRAB() (((stop != nullptr && xb_ld(stop) >= thr) || (quota > 0 && qleft-- <= 0)) ? (unsigned)hi : (unsigned)lo + atomicAdd(cnt, 1u))
;     ...
;         unsigned nxt = 0u; if (tid == 0) nxt = Q_GRAB();
;         signed char* Qc = Qp; float* csc = csp; const bool f8c = f8; const float qmax = f8c ? 448.0f : 127.0f, qinv = f8c ? (1.0f / 448.0f) : (1.0f / 127.0f);
;         f32x4 mx = {0.f, 0.f, 0.f, 0.f};
; #pragma unroll
;         for (int g = 0; g < 8; ++g)
; #pragma unroll
;             for (int r = 0; r < 4; ++r) { mx[0] = fmaxf(mx[0], fabsf(v[g][r][0])); mx[1] = fmaxf(mx[1], fabsf(v[g][r][1])); mx[2] = fmaxf(mx[2], fabsf(v[g][r][2])); mx[3] = fmaxf(mx[3], fabsf(v[g][r][3])); }
; #pragma unroll
;         for (int c = 0; c < 4; ++c) { float m = mx[c]; m = fmaxf(m, __shfl_xor(m, 8)); m = fmaxf(m, __shfl_xor(m, 16)); m = fmaxf(m, __shfl_xor(m, 32)); mx[c] = m; }
;         if (tid == 0) MISC[2] = nxt;
;         if (kr == 0) *(LAS f32x4*)(smax + wave * 32 + 4 * n4) = mx;
.LBB0_334:
	s_waitcnt vmcnt(10)
	v_max3_f32 v130, |v2|, 0, |v6|
	s_waitcnt vmcnt(8)
	v_max3_f32 v130, v130, |v10|, |v14|
	v_max3_f32 v130, v130, |v18|, |v22|
	v_max3_f32 v130, v130, |v26|, |v30|
	v_max3_f32 v130, v130, |v34|, |v38|
	v_max3_f32 v130, v130, |v42|, |v46|
	v_max3_f32 v131, |v3|, 0, |v7|
	v_max3_f32 v130, v130, |v50|, |v54|
	v_max3_f32 v132, |v4|, 0, |v8|
	v_max3_f32 v131, v131, |v11|, |v15|
	v_max3_f32 v130, v130, |v58|, |v62|
	v_max3_f32 v132, v132, |v12|, |v16|
	v_max3_f32 v131, v131, |v19|, |v23|
	v_max3_f32 v130, v130, |v66|, |v70|
	v_max3_f32 v132, v132, |v20|, |v24|
	v_max3_f32 v131, v131, |v27|, |v31|
	v_max3_f32 v130, v130, |v74|, |v78|
	v_max3_f32 v132, v132, |v28|, |v32|
	v_max3_f32 v131, v131, |v35|, |v39|
	v_max3_f32 v130, v130, |v82|, |v86|
	v_max3_f32 v132, v132, |v36|, |v40|
	v_max3_f32 v131, v131, |v43|, |v47|
	v_max3_f32 v130, v130, |v90|, |v94|
	v_max3_f32 v132, v132, |v44|, |v48|
	v_max3_f32 v131, v131, |v51|, |v55|
	s_waitcnt vmcnt(6)
	v_max3_f32 v130, v130, |v98|, |v102|
	v_max3_f32 v133, |v5|, 0, |v9|
	v_max3_f32 v132, v132, |v52|, |v56|
	v_max3_f32 v131, v131, |v59|, |v63|
	s_waitcnt vmcnt(4)
	v_max3_f32 v130, v130, |v106|, |v110|
	v_max3_f32 v133, v133, |v13|, |v17|
	v_max3_f32 v132, v132, |v60|, |v64|
	v_max3_f32 v131, v131, |v67|, |v71|
	s_waitcnt vmcnt(2)
	v_max3_f32 v130, v130, |v114|, |v118|
	v_max3_f32 v133, v133, |v21|, |v25|
	v_max3_f32 v132, v132, |v68|, |v72|
	v_max3_f32 v131, v131, |v75|, |v79|
	s_waitcnt vmcnt(0)
	v_max3_f32 v130, v130, |v122|, |v126|
	v_max3_f32 v133, v133, |v29|, |v33|
	v_max3_f32 v132, v132, |v76|, |v80|
	v_max3_f32 v131, v131, |v83|, |v87|
	v_max3_f32 v133, v133, |v37|, |v41|
	v_max3_f32 v132, v132, |v84|, |v88|
	v_max3_f32 v131, v131, |v91|, |v95|
	v_max3_f32 v133, v133, |v45|, |v49|
	v_max3_f32 v132, v132, |v92|, |v96|
	v_max3_f32 v131, v131, |v99|, |v103|
	v_max3_f32 v133, v133, |v53|, |v57|
	v_max3_f32 v132, v132, |v100|, |v104|
	v_max3_f32 v131, v131, |v107|, |v111|
	v_max3_f32 v133, v133, |v61|, |v65|
	v_max3_f32 v132, v132, |v108|, |v112|
	v_max3_f32 v131, v131, |v115|, |v119|
	v_max3_f32 v133, v133, |v69|, |v73|
	v_max3_f32 v132, v132, |v116|, |v120|
	v_max3_f32 v131, v131, |v123|, |v127|
	v_max3_f32 v133, v133, |v77|, |v81|
	v_max3_f32 v135, v132, |v124|, |v128|
	v_max3_f32 v133, v133, |v85|, |v89|
	v_max3_f32 v133, v133, |v93|, |v97|
	v_max3_f32 v133, v133, |v101|, |v105|
	v_max3_f32 v133, v133, |v109|, |v113|
	v_max3_f32 v133, v133, |v117|, |v121|
	v_max3_f32 v133, v133, |v125|, |v129|
	v_mov_b32_e32 v132, v135
	s_nop 1
	v_max_f32_dpp v130, v130, v130 row_ror:8 row_mask:0xf bank_mask:0xf
	v_max_f32_dpp v131, v131, v131 row_ror:8 row_mask:0xf bank_mask:0xf
	v_max_f32_dpp v132, v132, v132 row_ror:8 row_mask:0xf bank_mask:0xf
	v_max_f32_dpp v133, v133, v133 row_ror:8 row_mask:0xf bank_mask:0xf
	v_mov_b32_e32 v134, v130
	v_mov_b32_e32 v136, v131
	v_mov_b32_e32 v137, v132
	v_mov_b32_e32 v138, v133
	s_nop 1
	v_permlane16_swap_b32 v130, v134
	v_permlane16_swap_b32 v131, v136
	v_permlane16_swap_b32 v132, v137
	v_permlane16_swap_b32 v133, v138
	v_max_f32_e32 v130, v130, v134
	v_max_f32_e32 v131, v131, v136
	v_max_f32_e32 v132, v132, v137
	v_max_f32_e32 v133, v133, v138
	v_mov_b32_e32 v134, v130
	v_mov_b32_e32 v136, v131
	v_mov_b32_e32 v137, v132
	v_mov_b32_e32 v138, v133
	s_nop 1
	v_permlane32_swap_b32 v130, v134
	v_permlane32_swap_b32 v131, v136
	v_permlane32_swap_b32 v132, v137
	v_permlane32_swap_b32 v133, v138
	v_max_f32_e32 v130, v130, v134
	v_max_f32_e32 v131, v131, v136
	v_max_f32_e32 v132, v132, v137
	v_max_f32_e32 v133, v133, v138
	s_and_saveexec_b64 s[6:7], s[40:41]
	v_add_u32_e32 v1, 0x1c8, v199
	v_cmp_lt_u32_e32 vcc, 4, v201
	s_mov_b64 s[12:13], vcc
	v_cmp_le_u32_e32 vcc, 0x19c8, v1
	s_or_b64 s[12:13], s[12:13], vcc
	v_mov_b32_e32 v199, 0x1800
	s_andn2_b64 exec, exec, s[12:13]
	v_mov_b32_e32 v203, 1
	global_atomic_add v199, v171, v203, s[20:21] sc0
	s_and_b64 exec, s[6:7], s[40:41]
	global_load_dword v201, v171, s[22:23] sc1
	v_mov_b32_e32 v138, s75
	ds_write_b32 v138, v1
	s_or_b64 exec, exec, s[6:7]
	s_and_saveexec_b64 s[6:7], s[4:5]
	s_cbranch_execz .LBB0_343
	v_add_u32_e32 v1, s44, v169
	ds_write_b128 v1, v[130:133]
